# layer-1 prep row loop: rope-key loads requested at the top of the row with the other loads (one memory round trip per row instead of three)
# baseline (speedup 1.0000x reference)
; __device__ __forceinline__ unsigned cvtpk(float lo, float hi) { unsigned r; asm volatile("v_cvt_pk_bf16_f32 %0, %1, %2" : "=v"(r) : "v"(lo), "v"(hi)); return r; }
; __device__ __forceinline__ float bf2f(unsigned short b) { return __uint_as_float(((unsigned)b) << 16); }
; __device__ __forceinline__ void phase_prep_mla(bf16_t* H1, bf16_t* krope, unsigned char* kr8, int G, int bid, int tid) {
;     ...
;     for (int m = bid * 8 + wid; m < T_; m += G * 8) {
;         bf16_t* rowp = H1 + (size_t)m * IN1P;
;         const u32x4 a = *(const u32x4*)(rowp + 3072 + lane * 8);
;         float ss = bflo(a.x) * bflo(a.x) + bfhi(a.x) * bfhi(a.x) + bflo(a.y) * bflo(a.y) + bfhi(a.y) * bfhi(a.y) + bflo(a.z) * bflo(a.z) + bfhi(a.z) * bfhi(a.z) + bflo(a.w) * bflo(a.w) + bfhi(a.w) * bfhi(a.w);
;         ss = wave_sum(ss);
;         const u32x2 c = *(const u32x2*)(rowp + 3584 + lane * 4);
;         float s2 = bflo(c.x) * bflo(c.x) + bfhi(c.x) * bfhi(c.x) + bflo(c.y) * bflo(c.y) + bfhi(c.y) * bfhi(c.y);
;         s2 = wave_sum(s2);
;         const float rq = rsqrtf(ss * (1.0f / 512.0f) + 1e-6f), rkv = rsqrtf(s2 * (1.0f / 256.0f) + 1e-6f);
;         if constexpr (F8_P3 != 0) {
;             *(u32x2*)((unsigned char*)(rowp + 3072) + lane * 8) = (u32x2){pk4_fp8(bflo(a.x) * rq, bfhi(a.x) * rq, bflo(a.y) * rq, bfhi(a.y) * rq), pk4_fp8(bflo(a.z) * rq, bfhi(a.z) * rq, bflo(a.w) * rq, bfhi(a.w) * rq)};
;             *(unsigned*)((unsigned char*)(rowp + 3584) + lane * 4) = pk4_fp8(bflo(c.x) * rkv, bfhi(c.x) * rkv, bflo(c.y) * rkv, bfhi(c.y) * rkv); }
;         else {
;         *(u32x4*)(rowp + 3072 + lane * 8) = (u32x4){cvtpk(bflo(a.x) * rq, bfhi(a.x) * rq), cvtpk(bflo(a.y) * rq, bfhi(a.y) * rq), cvtpk(bflo(a.z) * rq, bfhi(a.z) * rq), cvtpk(bflo(a.w) * rq, bfhi(a.w) * rq)};
;         *(u32x2*)(rowp + 3584 + lane * 4) = (u32x2){cvtpk(bflo(c.x) * rkv, bfhi(c.x) * rkv), cvtpk(bflo(c.y) * rkv, bfhi(c.y) * rkv)}; }
;         if (lane < 32) { const float x1 = bf2f(rowp[3840 + lane]), x2 = bf2f(rowp[3840 + 32 + lane]);
;             float sn, cs; sincos_rev((float)(m & (SEQ - 1)) * invf, sn, cs);
;             const float o1 = x1 * cs - x2 * sn, o2 = x2 * cs + x1 * sn;
;             krope[(size_t)m * 64 + lane] = f2bf(o1); krope[(size_t)m * 64 + 32 + lane] = f2bf(o2);
;             if (F8_ATTD) { kr8[(size_t)m * 64 + lane] = f2fp8(o1); kr8[(size_t)m * 64 + 32 + lane] = f2fp8(o2); } }
.LBB0_223:
	s_waitcnt lgkmcnt(0)
	v_lshl_add_u64 v[12:13], s[2:3], 0, v[4:5]
	global_load_dwordx4 v[12:15], v[12:13], off
	v_lshl_add_u64 v[22:23], s[2:3], 0, v[6:7]
	s_mov_b32 s0, 0x24601000
	v_add_co_u32_e32 v22, vcc, s0, v22
	s_mov_b32 s0, 0x3b800000
	s_nop 0
	v_addc_co_u32_e32 v23, vcc, 0, v23, vcc
	global_load_dwordx2 v[24:25], v[22:23], off offset:3072
	v_lshl_add_u64 v[178:179], s[2:3], 0, v[10:11]
	v_add_co_u32_e32 v178, vcc, 0x24601000, v178
	s_nop 1
	v_addc_co_u32_e32 v179, vcc, 0, v179, vcc
	global_load_ushort v176, v[178:179], off offset:3584
	global_load_ushort v177, v[178:179], off offset:3648
	s_mov_b32 s1, 0x3b000000
	s_waitcnt vmcnt(0)
	v_and_b32_e32 v32, 0xffff0000, v12
	v_lshlrev_b32_e32 v21, 16, v12
	v_mul_f32_e32 v18, v32, v32
	v_fmac_f32_e32 v18, v21, v21
	v_lshlrev_b32_e32 v33, 16, v13
	v_fmac_f32_e32 v18, v33, v33
	v_and_b32_e32 v34, 0xffff0000, v13
	v_and_b32_e32 v12, 0xffff0000, v14
	v_lshlrev_b32_e32 v13, 16, v14
	v_fmac_f32_e32 v18, v34, v34
	v_pk_mul_f32 v[16:17], v[12:13], v[12:13]
	v_lshlrev_b32_e32 v26, 16, v24
	v_add_f32_e32 v14, v17, v18
	v_add_f32_e32 v18, v16, v14
	v_and_b32_e32 v14, 0xffff0000, v15
	v_lshlrev_b32_e32 v15, 16, v15
	v_pk_mul_f32 v[16:17], v[14:15], v[14:15]
	v_and_b32_e32 v27, 0xffff0000, v24
	v_add_f32_e32 v17, v17, v18
	v_add_f32_e32 v16, v16, v17
	ds_swizzle_b32 v17, v16 offset:swizzle(SWAP,1)
	v_pk_mul_f32 v[28:29], v[26:27], v[26:27]
	v_and_b32_e32 v24, 0xffff0000, v25
	v_lshlrev_b32_e32 v25, 16, v25
	v_pk_mul_f32 v[30:31], v[24:25], v[24:25]
	s_waitcnt lgkmcnt(0)
	v_add_f32_e32 v16, v16, v17
	ds_swizzle_b32 v17, v16 offset:swizzle(SWAP,2)
	s_waitcnt lgkmcnt(0)
	v_add_f32_e32 v16, v16, v17
	ds_swizzle_b32 v17, v16 offset:swizzle(SWAP,4)
	s_waitcnt lgkmcnt(0)
	v_add_f32_e32 v16, v16, v17
	ds_swizzle_b32 v17, v16 offset:swizzle(SWAP,8)
	s_waitcnt lgkmcnt(0)
	v_add_f32_e32 v16, v16, v17
	ds_swizzle_b32 v17, v16 offset:swizzle(SWAP,16)
	s_waitcnt lgkmcnt(0)
	v_add_f32_e32 v17, v16, v17
	v_add_f32_e32 v16, v28, v29
	v_add_f32_e32 v16, v31, v16
	v_add_f32_e32 v16, v30, v16
	ds_swizzle_b32 v18, v16 offset:swizzle(SWAP,1)
	v_mov_b32_e32 v19, v17
	s_nop 1
	v_permlane32_swap_b32_e32 v17, v19
	s_waitcnt lgkmcnt(0)
	v_add_f32_e32 v16, v16, v18
	ds_swizzle_b32 v18, v16 offset:swizzle(SWAP,2)
	s_waitcnt lgkmcnt(0)
	v_add_f32_e32 v16, v16, v18
	ds_swizzle_b32 v18, v16 offset:swizzle(SWAP,4)
	s_waitcnt lgkmcnt(0)
	v_add_f32_e32 v16, v16, v18
	ds_swizzle_b32 v18, v16 offset:swizzle(SWAP,8)
	s_waitcnt lgkmcnt(0)
	v_add_f32_e32 v16, v16, v18
	ds_swizzle_b32 v18, v16 offset:swizzle(SWAP,16)
	s_waitcnt lgkmcnt(0)
	v_add_f32_e32 v16, v16, v18
	v_mov_b32_e32 v18, v16
	s_nop 1
	v_permlane32_swap_b32_e32 v16, v18
	v_pk_add_f32 v[16:17], v[16:17], v[18:19]
	v_mov_b32_e32 v18, 0x358637bd
	v_pk_fma_f32 v[16:17], v[16:17], s[0:1], v[18:19] op_sel_hi:[1,1,0]
	s_nop 0
	v_mul_f32_e32 v18, 0x4b800000, v17
	v_cmp_gt_f32_e64 s[40:41], s91, v17
	v_cmp_gt_f32_e32 vcc, s91, v16
	s_nop 0
	v_cndmask_b32_e64 v17, v17, v18, s[40:41]
	v_rsq_f32_e32 v17, v17
	s_nop 0
	v_mul_f32_e32 v18, 0x45800000, v17
	v_cndmask_b32_e64 v18, v17, v18, s[40:41]
	v_mul_f32_e32 v17, 0x4b800000, v16
	v_cndmask_b32_e32 v16, v16, v17, vcc
	v_rsq_f32_e32 v16, v16
	v_mul_f32_e32 v12, v18, v12
	v_mul_f32_e32 v14, v18, v14
	v_mul_f32_e32 v28, v18, v34
	v_mul_f32_e32 v17, 0x45800000, v16
	v_cndmask_b32_e32 v19, v16, v17, vcc
	v_mul_f32_e32 v16, v18, v21
	v_mul_f32_e32 v17, v18, v32
	v_cvt_pk_fp8_f32 v16, v16, v17
	v_mul_f32_e32 v17, v18, v13
	v_cvt_pk_fp8_f32 v17, v17, v12
	v_mul_f32_e32 v13, v18, v15
	v_mul_f32_e32 v12, v19, v27
	v_mul_f32_e32 v21, v18, v33
	v_cvt_pk_fp8_f32 v17, v13, v14 op_sel:[0,0,1]
	v_mul_f32_e32 v14, v19, v26
	v_cvt_pk_fp8_f32 v14, v14, v12
	v_mul_f32_e32 v13, v19, v25
	v_mul_f32_e32 v15, v19, v24
	v_cvt_pk_fp8_f32 v16, v21, v28 op_sel:[0,0,1]
	v_cvt_pk_fp8_f32 v14, v13, v15 op_sel:[0,0,1]
	v_lshl_add_u64 v[12:13], s[2:3], 0, v[8:9]
	global_store_dwordx2 v[22:23], v[16:17], off offset:2048
	global_store_dword v[12:13], v14, off
	s_and_saveexec_b64 s[0:1], s[38:39]
	s_cbranch_execz .LBB0_222
	s_and_b32 s7, s6, 0xfff
	v_lshlrev_b32_e32 v14, 16, v176
	v_cvt_f32_u32_e32 v13, s7
	s_mov_b32 s7, 0xa00000
	v_mul_f32_e32 v13, v20, v13
	v_mul_f32_e32 v15, 0.15915494, v13
	v_floor_f32_e32 v15, v15
	v_fma_f32 v13, v13, 0.15915494, -v15
	v_sin_f32_e32 v15, v13
	v_cos_f32_e32 v13, v13
	v_lshlrev_b32_e32 v12, 16, v177
	v_mul_f32_e32 v16, v15, v12
	v_fma_f32 v16, v13, v14, -v16
	v_mul_f32_e32 v17, v13, v12
	v_lshl_add_u64 v[12:13], s[2:3], 0, v[0:1]
	v_add_co_u32_e32 v12, vcc, s7, v12
	v_fmac_f32_e32 v17, v15, v14
	v_cvt_pk_bf16_f32 v14, v16, v16
	s_nop 0
	v_addc_co_u32_e32 v13, vcc, 0, v13, vcc
	global_store_short v[12:13], v14, off
	v_cvt_pk_bf16_f32 v14, v17, v17
	v_cvt_pk_fp8_f32 v16, v16, v16
	v_cvt_pk_fp8_f32 v17, v17, v17
	global_store_short v[12:13], v14, off offset:64
	v_lshl_add_u64 v[12:13], s[2:3], 0, v[2:3]
	v_add_co_u32_e32 v12, vcc, 0x1a200000, v12
	s_nop 1
	v_addc_co_u32_e32 v13, vcc, 0, v13, vcc
	global_store_byte v[12:13], v16, off
	global_store_byte v[12:13], v17, off offset:32
	s_branch .LBB0_222
